# v7: v6 + GLA-scan o-part issues its 8 LDS state-tile reads up front with counted lgkmcnt
# speedup vs baseline: 1.0056x; 1.0056x over previous
; __device__ __forceinline__ unsigned cvt_pk_bf16(float lo, float hi) { const f32x2_t v = {lo, hi}; return __builtin_bit_cast(unsigned, __builtin_convertvector(v, bf16x2_t)); }
; __device__ __forceinline__ void ph_glascan(const Params& p, float* lds, int wg, int nwg, int gct_begin) {
;     ...
;             GLA_LOAD_S(nkh, nvt, ndec, c + 1);
;             bf16_t* STc = (c & 1) ? ST1 : ST0; bf16_t* STn = (c & 1) ? ST0 : ST1;
; #pragma unroll
;             for (int dt = 0; dt < 2; ++dt)
; #pragma unroll
;                 for (int v2 = 0; v2 < 2; ++v2) {
;                     pg8::f32x4 a = acc[dt][v2] * cdec[dt];
; #pragma unroll
;                     for (int ks = 0; ks < 2; ++ks) a = __builtin_amdgcn_mfma_f32_16x16x32_bf16(ckh[dt][ks], cvt[v2][ks], a, 0, 0, 0);
;                     acc[dt][v2] = a;
;                     uint2 sv; sv.x = cvt_pk_bf16(a[0], a[1]); sv.y = cvt_pk_bf16(a[2], a[3]);
;                     *(uint2*)(STn + (v2 * 16 + r) * GLA_LDP + (2 * w + dt) * 16 + 4 * g) = sv;
;                 }
;             if (c >= 4) {
;                 pg8::f32x4 o = {0.f, 0.f, 0.f, 0.f};
; #pragma unroll
;                 for (int ks = 0; ks < 8; ++ks) { const pg8::bf16x8 sa = *(const pg8::bf16x8*)(STc + (vt * 16 + r) * GLA_LDP + ks * 32 + 8 * g);
;                     o = __builtin_amdgcn_mfma_f32_16x16x32_bf16(sa, cqt[ks], o, 0, 0, 0); }
;                 if (vt == 0) {
; #pragma unroll
;                     for (int ks = 0; ks < 2; ++ks) o = __builtin_amdgcn_mfma_f32_16x16x32_bf16(cvt[0][ks], cam[ks], o, 0, 0, 0);
;                 } else {
; #pragma unroll
;                     for (int ks = 0; ks < 2; ++ks) o = __builtin_amdgcn_mfma_f32_16x16x32_bf16(cvt[1][ks], cam[ks], o, 0, 0, 0);
;                 }
.LBB0_1616:
	v_lshl_add_u64 v[4:5], v[180:181], 0, s[54:55]
	s_mov_b32 s25, 0x8000
	v_add_co_u32_e32 v4, vcc, s25, v4
	v_mov_b64_e32 v[210:211], v[16:17]
	v_mov_b64_e32 v[214:215], v[20:21]
	v_mov_b64_e32 v[218:219], v[12:13]
	v_mov_b64_e32 v[222:223], v[8:9]
	v_addc_co_u32_e32 v5, vcc, 0, v5, vcc
	v_mov_b64_e32 v[208:209], v[14:15]
	v_mov_b64_e32 v[212:213], v[18:19]
	v_mov_b64_e32 v[216:217], v[10:11]
	v_mov_b64_e32 v[220:221], v[6:7]
	global_load_dwordx4 v[14:17], v[4:5], off
	global_load_dwordx4 v[18:21], v[4:5], off offset:1024
	global_load_dwordx4 v[106:109], v[186:187], off
	global_load_dwordx4 v[110:113], v[186:187], off offset:1024
	global_load_dwordx4 v[10:13], v[4:5], off offset:2048
	global_load_dwordx4 v[6:9], v[4:5], off offset:3072
	global_load_dwordx4 v[122:125], v[186:187], off offset:2048
	global_load_dwordx4 v[118:121], v[186:187], off offset:3072
	v_mov_b64_e32 v[156:157], v[28:29]
	v_mov_b64_e32 v[152:153], v[24:25]
	v_mov_b64_e32 v[154:155], v[26:27]
	v_mov_b64_e32 v[150:151], v[22:23]
	v_pk_mul_f32 v[24:25], v[100:101], v[156:157]
	v_pk_mul_f32 v[22:23], v[98:99], v[154:155]
	v_pk_mul_f32 v[84:85], v[84:85], v[152:153]
	v_pk_mul_f32 v[82:83], v[82:83], v[150:151]
	v_mfma_f32_16x16x32_bf16 v[98:101], v[208:211], v[138:141], v[22:25]
	global_load_dwordx4 v[26:29], v[178:179], off
	s_nop 1
	global_load_dwordx4 v[22:25], v[178:179], off offset:64
	v_pk_mul_f32 v[92:93], v[92:93], v[156:157]
	v_pk_mul_f32 v[90:91], v[90:91], v[154:155]
	v_mfma_f32_16x16x32_bf16 v[82:85], v[216:219], v[138:141], v[82:85]
	v_mul_f32_e64 v68, v68, v152
	v_mul_f32_e64 v69, v69, v153
	v_pk_mul_f32 v[66:67], v[66:67], v[150:151]
	s_bitcmp0_b32 s90, 0
	v_mfma_f32_16x16x32_bf16 v[90:93], v[208:211], v[146:149], v[90:93]
	s_cselect_b64 s[56:57], -1, 0
	s_and_b64 s[58:59], s[56:57], exec
	s_cselect_b32 s25, s5, 0
	v_mfma_f32_16x16x32_bf16 v[66:69], v[216:219], v[146:149], v[66:69]
	s_add_i32 s25, s25, s70
	v_add3_u32 v2, s25, v162, v197
	s_cmp_lt_u32 s90, 4
	v_mfma_f32_16x16x32_bf16 v[98:101], v[212:215], v[134:137], v[98:101]
	v_mfma_f32_16x16x32_bf16 v[82:85], v[220:223], v[134:137], v[82:85]
	v_mfma_f32_16x16x32_bf16 v[90:93], v[212:215], v[142:145], v[90:93]
	s_nop 5
	v_cvt_pk_bf16_f32 v4, v98, v99
	v_cvt_pk_bf16_f32 v5, v100, v101
	v_cvt_pk_bf16_f32 v150, v82, v83
	v_mfma_f32_16x16x32_bf16 v[66:69], v[220:223], v[142:145], v[66:69]
	v_cvt_pk_bf16_f32 v151, v84, v85
	v_cvt_pk_bf16_f32 v154, v90, v91
	v_cvt_pk_bf16_f32 v155, v92, v93
	ds_write2_b64 v2, v[4:5], v[150:151] offset1:4
	v_add_u32_e32 v2, 0x2000, v2
	s_nop 2
	v_cvt_pk_bf16_f32 v4, v66, v67
	v_cvt_pk_bf16_f32 v5, v68, v69
	ds_write2_b64 v2, v[154:155], v[4:5] offset0:32 offset1:36
	s_cbranch_scc1 .LBB0_1623
	s_and_b64 s[56:57], s[56:57], exec
	s_cselect_b32 s25, 0, s5
	v_lshlrev_b32_e32 v2, 1, v162
	v_add3_u32 v2, s25, v196, v2
	ds_read_b128 v[150:153], v2
	ds_read_b128 v[154:157], v2 offset:64
	ds_read_b128 v[224:227], v2 offset:128
	ds_read_b128 v[228:231], v2 offset:192
	ds_read_b128 v[232:235], v2 offset:256
	ds_read_b128 v[236:239], v2 offset:320
	ds_read_b128 v[240:243], v2 offset:384
	s_mov_b64 s[56:57], -1
	s_andn2_b64 vcc, exec, s[82:83]
	s_waitcnt lgkmcnt(5)
	s_cmp_lt_i32 s90, s69
	s_cbranch_scc1 .Lgla_o_ok
	s_waitcnt vmcnt(10)
.Lgla_o_ok:
	v_mfma_f32_16x16x32_bf16 v[150:153], v[150:153], v[62:65], 0
	v_mfma_f32_16x16x32_bf16 v[150:153], v[154:157], v[58:61], v[150:153]
	ds_read_b128 v[154:157], v2 offset:448
	s_waitcnt lgkmcnt(5)
	v_mfma_f32_16x16x32_bf16 v[150:153], v[224:227], v[54:57], v[150:153]
	s_waitcnt lgkmcnt(4)
	v_mfma_f32_16x16x32_bf16 v[150:153], v[228:231], v[46:49], v[150:153]
	s_waitcnt lgkmcnt(3)
	v_mfma_f32_16x16x32_bf16 v[150:153], v[232:235], v[50:53], v[150:153]
	s_waitcnt lgkmcnt(2)
	v_mfma_f32_16x16x32_bf16 v[150:153], v[236:239], v[42:45], v[150:153]
	s_waitcnt lgkmcnt(1)
	v_mfma_f32_16x16x32_bf16 v[150:153], v[240:243], v[38:41], v[150:153]
	s_waitcnt lgkmcnt(0)
	v_mfma_f32_16x16x32_bf16 v[150:153], v[154:157], v[34:37], v[150:153]
	s_cbranch_vccnz .LBB0_1619
	v_mfma_f32_16x16x32_bf16 v[146:149], v[146:149], v[30:33], v[150:153]
	s_mov_b64 s[56:57], 0
	v_mfma_f32_16x16x32_bf16 v[154:157], v[142:145], v[70:73], v[146:149]
